# P9 epilogue: one-line touch loads pull the residual rows of chunks 2..7 towards the caches at the start of the epilogue (latency-bound chunk ladder)
# baseline (speedup 1.0000x reference)
.LBB0_1188:
	v_lshl_add_u32 v146, s26, 8, v1
	v_ashrrev_i32_e32 v147, 31, v146
	v_lshl_or_b32 v182, s58, 8, v224
	v_lshl_add_u64 v[178:179], v[146:147], 2, s[4:5]
	v_ashrrev_i32_e32 v183, 31, v182
	global_load_dword v180, v[178:179], off
	v_lshlrev_b64 v[148:149], 2, v[182:183]
	v_lshlrev_b64 v[150:151], 14, v[146:147]
	v_or_b32_e32 v186, 16, v146
	v_lshl_add_u64 v[110:111], s[8:9], 0, v[148:149]
	v_lshl_add_u64 v[150:151], s[0:1], 0, v[150:151]
	v_ashrrev_i32_e32 v187, 31, v186
	global_load_dwordx4 v[126:129], v[110:111], off nt
	global_load_dwordx4 v[122:125], v[110:111], off offset:16 nt
	global_load_dwordx4 v[106:109], v[110:111], off offset:528 nt
	s_nop 0
	global_load_dwordx4 v[110:113], v[110:111], off offset:512 nt
	v_lshl_add_u64 v[162:163], v[150:151], 0, v[148:149]
	v_mov_b32_e32 v248, v162
	v_mov_b32_e32 v249, v163
	v_lshlrev_b64 v[166:167], 14, v[186:187]
	global_load_dwordx4 v[150:153], v[162:163], off nt
	global_load_dwordx4 v[154:157], v[162:163], off offset:16 nt
	global_load_dwordx4 v[158:161], v[162:163], off offset:512 nt
	s_nop 0
	global_load_dwordx4 v[162:165], v[162:163], off offset:528 nt
	s_nop 0
	global_load_dword v184, v[178:179], off offset:64
	v_lshl_add_u64 v[166:167], s[0:1], 0, v[166:167]
	v_lshl_add_u64 v[174:175], v[166:167], 0, v[148:149]
	global_load_dwordx4 v[166:169], v[174:175], off nt
	global_load_dwordx4 v[170:173], v[174:175], off offset:16 nt
	v_cvt_f32_i32_e32 v189, v143
	v_cvt_f32_i32_e32 v188, v142
	v_cvt_f32_i32_e32 v191, v145
	v_cvt_f32_i32_e32 v190, v144
	global_load_dwordx4 v[142:145], v[174:175], off offset:528 nt
	s_nop 0
	global_load_dwordx4 v[174:177], v[174:175], off offset:512 nt
	v_and_b32_e32 v250, 63, v0
	v_bfe_u32 v251, v250, 4, 1
	v_lshrrev_b32_e32 v250, 5, v250
	v_lshlrev_b32_e32 v251, 9, v251
	v_lshl_or_b32 v251, v250, 18, v251
	v_mov_b32_e32 v253, 0
	v_add_u32_e32 v252, 0x80000, v251
	v_lshl_add_u64 v[254:255], v[252:253], 0, v[248:249]
	global_load_dword v250, v[254:255], off
	v_add_u32_e32 v252, 0x200000, v251
	v_lshl_add_u64 v[254:255], v[252:253], 0, v[248:249]
	global_load_dword v250, v[254:255], off
	v_add_u32_e32 v252, 0x280000, v251
	v_lshl_add_u64 v[254:255], v[252:253], 0, v[248:249]
	global_load_dword v250, v[254:255], off
	v_cvt_f32_i32_e32 v193, v139
	v_cvt_f32_i32_e32 v192, v138
	v_cvt_f32_i32_e32 v213, v141
	v_cvt_f32_i32_e32 v212, v140
	v_cvt_f32_i32_e32 v215, v135
	v_cvt_f32_i32_e32 v214, v134
	v_cvt_f32_i32_e32 v217, v137
	v_cvt_f32_i32_e32 v216, v136
	v_cvt_f32_i32_e32 v219, v131
	v_cvt_f32_i32_e32 v218, v130
	v_cvt_f32_i32_e32 v221, v133
	v_cvt_f32_i32_e32 v220, v132
	v_or_b32_e32 v222, 32, v146
	v_lshlrev_b64 v[228:229], 13, v[146:147]
	v_cvt_f32_i32_e32 v119, v119
	v_cvt_f32_i32_e32 v118, v118
	v_lshlrev_b64 v[130:131], 1, v[182:183]
	v_ashrrev_i32_e32 v223, 31, v222
	global_load_dword v182, v[178:179], off offset:128
	global_load_dword v140, v[178:179], off offset:192
	global_load_dword v138, v[178:179], off offset:512
	global_load_dword v136, v[178:179], off offset:576
	global_load_dword v134, v[178:179], off offset:640
	global_load_dword v132, v[178:179], off offset:704
	v_lshl_add_u64 v[178:179], s[10:11], 0, v[228:229]
	v_cvt_f32_i32_e32 v115, v115
	v_cvt_f32_i32_e32 v117, v117
	v_cvt_f32_i32_e32 v116, v116
	v_cvt_f32_i32_e32 v114, v114
	v_lshlrev_b64 v[228:229], 14, v[222:223]
	v_lshl_add_u64 v[178:179], v[178:179], 0, v[130:131]
	v_lshl_add_u64 v[228:229], s[0:1], 0, v[228:229]
	v_cvt_f32_i32_e32 v121, v121
	v_cvt_f32_i32_e32 v120, v120
	v_lshl_add_u64 v[228:229], v[228:229], 0, v[148:149]
	v_cvt_f32_i32_e32 v103, v103
	v_cvt_f32_i32_e32 v102, v102
	v_cvt_f32_i32_e32 v101, v101
	v_cvt_f32_i32_e32 v100, v100
	v_cvt_f32_i32_e32 v105, v105
	v_cvt_f32_i32_e32 v104, v104
	v_cvt_f32_i32_e32 v99, v99
	v_cvt_f32_i32_e32 v98, v98
	v_cvt_f32_i32_e32 v97, v97
	v_cvt_f32_i32_e32 v96, v96
	v_cvt_f32_i32_e32 v87, v87
	v_cvt_f32_i32_e32 v86, v86
	v_cvt_f32_i32_e32 v89, v89
	v_cvt_f32_i32_e32 v88, v88
	v_cvt_f32_i32_e32 v83, v83
	v_cvt_f32_i32_e32 v85, v85
	v_cvt_f32_i32_e32 v84, v84
	v_cvt_f32_i32_e32 v82, v82
	v_cvt_f32_i32_e32 v79, v79
	v_cvt_f32_i32_e32 v78, v78
	v_cvt_f32_i32_e32 v75, v75
	v_cvt_f32_i32_e32 v77, v77
	v_cvt_f32_i32_e32 v76, v76
	v_cvt_f32_i32_e32 v74, v74
	v_cvt_f32_i32_e32 v81, v81
	v_cvt_f32_i32_e32 v80, v80
	v_cvt_f32_i32_e32 v71, v71
	v_cvt_f32_i32_e32 v70, v70
	v_cvt_f32_i32_e32 v67, v67
	v_cvt_f32_i32_e32 v69, v69
	v_cvt_f32_i32_e32 v68, v68
	v_cvt_f32_i32_e32 v66, v66
	v_cvt_f32_i32_e32 v73, v73
	v_cvt_f32_i32_e32 v72, v72
	v_cvt_f32_i32_e32 v63, v63
	s_waitcnt vmcnt(0)
	v_pk_mul_f32 v[230:231], v[180:181], v[126:127] op_sel_hi:[0,1]
	v_pk_mul_f32 v[232:233], v[180:181], v[128:129] op_sel_hi:[0,1]
	v_pk_mul_f32 v[234:235], v[180:181], v[122:123] op_sel_hi:[0,1]
	v_pk_mul_f32 v[236:237], v[180:181], v[124:125] op_sel_hi:[0,1]
	v_pk_fma_f32 v[152:153], v[232:233], v[190:191], v[152:153]
	v_pk_fma_f32 v[150:151], v[230:231], v[188:189], v[150:151]
	v_pk_mul_f32 v[238:239], v[180:181], v[110:111] op_sel_hi:[0,1]
	v_pk_mul_f32 v[240:241], v[180:181], v[112:113] op_sel_hi:[0,1]
	v_pk_mul_f32 v[242:243], v[180:181], v[106:107] op_sel_hi:[0,1]
	v_pk_mul_f32 v[180:181], v[180:181], v[108:109] op_sel_hi:[0,1]
	v_pk_fma_f32 v[156:157], v[236:237], v[212:213], v[156:157]
	v_pk_fma_f32 v[154:155], v[234:235], v[192:193], v[154:155]
	v_cvt_pk_bf16_f32 v150, v150, v151
	v_cvt_pk_bf16_f32 v151, v152, v153
	v_pk_fma_f32 v[160:161], v[240:241], v[216:217], v[160:161]
	v_cvt_pk_bf16_f32 v152, v154, v155
	v_cvt_pk_bf16_f32 v153, v156, v157
	v_pk_fma_f32 v[158:159], v[238:239], v[214:215], v[158:159]
	v_pk_fma_f32 v[164:165], v[180:181], v[220:221], v[164:165]
	v_pk_fma_f32 v[162:163], v[242:243], v[218:219], v[162:163]
	global_store_dwordx4 v[178:179], v[150:153], off
	v_pk_mul_f32 v[188:189], v[184:185], v[122:123] op_sel_hi:[0,1]
	v_pk_mul_f32 v[190:191], v[184:185], v[124:125] op_sel_hi:[0,1]
	v_cvt_pk_bf16_f32 v150, v158, v159
	v_cvt_pk_bf16_f32 v151, v160, v161
	v_cvt_pk_bf16_f32 v152, v162, v163
	v_cvt_pk_bf16_f32 v153, v164, v165
	global_store_dwordx4 v[178:179], v[150:153], off offset:256
	v_pk_mul_f32 v[178:179], v[184:185], v[126:127] op_sel_hi:[0,1]
	v_pk_fma_f32 v[118:119], v[178:179], v[118:119], v[166:167]
	global_load_dwordx4 v[150:153], v[228:229], off offset:16 nt
	global_load_dwordx4 v[154:157], v[228:229], off nt
	global_load_dwordx4 v[158:161], v[228:229], off offset:528 nt
	global_load_dwordx4 v[162:165], v[228:229], off offset:512 nt
	v_pk_fma_f32 v[166:167], v[190:191], v[116:117], v[172:173]
	v_pk_fma_f32 v[116:117], v[188:189], v[114:115], v[170:171]
	v_cvt_pk_bf16_f32 v114, v118, v119
	v_lshlrev_b64 v[118:119], 13, v[186:187]
	v_pk_mul_f32 v[180:181], v[184:185], v[128:129] op_sel_hi:[0,1]
	v_lshl_add_u64 v[118:119], s[10:11], 0, v[118:119]
	v_pk_fma_f32 v[120:121], v[180:181], v[120:121], v[168:169]
	v_lshl_add_u64 v[118:119], v[118:119], 0, v[130:131]
	v_cvt_pk_bf16_f32 v115, v120, v121
	v_cvt_pk_bf16_f32 v116, v116, v117
	v_cvt_pk_bf16_f32 v117, v166, v167
	global_store_dwordx4 v[118:119], v[114:117], off
	v_pk_mul_f32 v[166:167], v[184:185], v[108:109] op_sel_hi:[0,1]
	v_pk_mul_f32 v[120:121], v[184:185], v[106:107] op_sel_hi:[0,1]
	v_pk_mul_f32 v[114:115], v[184:185], v[110:111] op_sel_hi:[0,1]
	v_pk_mul_f32 v[116:117], v[184:185], v[112:113] op_sel_hi:[0,1]
	v_pk_fma_f32 v[102:103], v[114:115], v[102:103], v[174:175]
	v_pk_fma_f32 v[114:115], v[166:167], v[100:101], v[144:145]
	v_or_b32_e32 v166, 48, v146
	v_pk_fma_f32 v[104:105], v[116:117], v[104:105], v[176:177]
	v_pk_fma_f32 v[100:101], v[120:121], v[98:99], v[142:143]
	v_cvt_pk_bf16_f32 v98, v102, v103
	v_cvt_pk_bf16_f32 v99, v104, v105
	v_ashrrev_i32_e32 v167, 31, v166
	v_cvt_pk_bf16_f32 v100, v100, v101
	v_cvt_pk_bf16_f32 v101, v114, v115
	global_store_dwordx4 v[118:119], v[98:101], off offset:256
	v_cvt_f32_i32_e32 v119, v95
	v_cvt_f32_i32_e32 v118, v94
	v_lshlrev_b64 v[98:99], 14, v[166:167]
	v_lshl_add_u64 v[98:99], s[0:1], 0, v[98:99]
	v_lshl_add_u64 v[114:115], v[98:99], 0, v[148:149]
	global_load_dwordx4 v[98:101], v[114:115], off nt
	global_load_dwordx4 v[102:105], v[114:115], off offset:16 nt
	v_cvt_f32_i32_e32 v143, v93
	v_cvt_f32_i32_e32 v142, v92
	global_load_dwordx4 v[92:95], v[114:115], off offset:528 nt
	s_nop 0
	global_load_dwordx4 v[114:117], v[114:115], off offset:512 nt
	v_cvt_f32_i32_e32 v121, v91
	v_cvt_f32_i32_e32 v120, v90
	v_lshlrev_b64 v[144:145], 13, v[222:223]
	v_pk_mul_f32 v[168:169], v[182:183], v[126:127] op_sel_hi:[0,1]
	v_lshl_add_u64 v[144:145], s[10:11], 0, v[144:145]
	v_pk_mul_f32 v[170:171], v[182:183], v[128:129] op_sel_hi:[0,1]
	v_pk_mul_f32 v[172:173], v[182:183], v[122:123] op_sel_hi:[0,1]
	v_lshl_add_u64 v[144:145], v[144:145], 0, v[130:131]
	v_pk_mul_f32 v[174:175], v[182:183], v[124:125] op_sel_hi:[0,1]
	v_add_u32_e32 v90, 0x80, v146
	v_pk_mul_f32 v[176:177], v[182:183], v[110:111] op_sel_hi:[0,1]
	v_pk_mul_f32 v[178:179], v[182:183], v[112:113] op_sel_hi:[0,1]
	v_ashrrev_i32_e32 v91, 31, v90
	v_cvt_f32_i32_e32 v62, v62
	v_cvt_f32_i32_e32 v59, v59
	v_cvt_f32_i32_e32 v61, v61
	v_cvt_f32_i32_e32 v60, v60
	v_cvt_f32_i32_e32 v58, v58
	v_cvt_f32_i32_e32 v65, v65
	v_cvt_f32_i32_e32 v64, v64
	v_cvt_f32_i32_e32 v55, v55
	v_cvt_f32_i32_e32 v54, v54
	v_cvt_f32_i32_e32 v53, v53
	v_cvt_f32_i32_e32 v52, v52
	v_cvt_f32_i32_e32 v57, v57
	v_cvt_f32_i32_e32 v56, v56
	v_cvt_f32_i32_e32 v51, v51
	v_cvt_f32_i32_e32 v50, v50
	v_cvt_f32_i32_e32 v47, v47
	v_cvt_f32_i32_e32 v46, v46
	v_cvt_f32_i32_e32 v43, v43
	v_cvt_f32_i32_e32 v45, v45
	v_cvt_f32_i32_e32 v44, v44
	v_cvt_f32_i32_e32 v42, v42
	v_cvt_f32_i32_e32 v49, v49
	v_cvt_f32_i32_e32 v48, v48
	v_cvt_f32_i32_e32 v39, v39
	v_cvt_f32_i32_e32 v38, v38
	v_cvt_f32_i32_e32 v37, v37
	v_cvt_f32_i32_e32 v36, v36
	s_waitcnt vmcnt(9)
	v_pk_fma_f32 v[120:121], v[172:173], v[120:121], v[150:151]
	s_waitcnt vmcnt(8)
	v_pk_fma_f32 v[118:119], v[168:169], v[118:119], v[154:155]
	v_pk_fma_f32 v[96:97], v[170:171], v[96:97], v[156:157]
	v_cvt_pk_bf16_f32 v118, v118, v119
	v_pk_fma_f32 v[142:143], v[174:175], v[142:143], v[152:153]
	v_cvt_pk_bf16_f32 v119, v96, v97
	v_cvt_pk_bf16_f32 v120, v120, v121
	v_pk_mul_f32 v[96:97], v[182:183], v[106:107] op_sel_hi:[0,1]
	v_cvt_pk_bf16_f32 v121, v142, v143
	global_store_dwordx4 v[144:145], v[118:121], off
	s_waitcnt vmcnt(7)
	v_pk_fma_f32 v[88:89], v[178:179], v[88:89], v[164:165]
	v_pk_fma_f32 v[86:87], v[176:177], v[86:87], v[162:163]
	v_pk_mul_f32 v[118:119], v[182:183], v[108:109] op_sel_hi:[0,1]
	v_pk_fma_f32 v[118:119], v[118:119], v[84:85], v[160:161]
	v_pk_fma_f32 v[84:85], v[96:97], v[82:83], v[158:159]
	v_cvt_pk_bf16_f32 v82, v86, v87
	v_cvt_pk_bf16_f32 v83, v88, v89
	v_pk_mul_f32 v[152:153], v[140:141], v[122:123] op_sel_hi:[0,1]
	v_cvt_pk_bf16_f32 v84, v84, v85
	v_cvt_pk_bf16_f32 v85, v118, v119
	global_store_dwordx4 v[144:145], v[82:85], off offset:256
	v_pk_mul_f32 v[154:155], v[140:141], v[124:125] op_sel_hi:[0,1]
	v_pk_mul_f32 v[150:151], v[140:141], v[128:129] op_sel_hi:[0,1]
	v_lshlrev_b64 v[82:83], 14, v[90:91]
	v_lshl_add_u64 v[82:83], s[0:1], 0, v[82:83]
	v_lshl_add_u64 v[96:97], v[82:83], 0, v[148:149]
	global_load_dwordx4 v[82:85], v[96:97], off nt
	global_load_dwordx4 v[86:89], v[96:97], off offset:16 nt
	global_load_dwordx4 v[118:121], v[96:97], off offset:528 nt
	global_load_dwordx4 v[142:145], v[96:97], off offset:512 nt
	v_pk_mul_f32 v[96:97], v[140:141], v[126:127] op_sel_hi:[0,1]
	v_cvt_f32_i32_e32 v41, v41
	v_cvt_f32_i32_e32 v40, v40
	v_cvt_f32_i32_e32 v35, v35
	v_cvt_f32_i32_e32 v34, v34
	v_cvt_f32_i32_e32 v31, v31
	v_cvt_f32_i32_e32 v30, v30
	v_cvt_f32_i32_e32 v27, v27
	s_waitcnt vmcnt(9)
	v_pk_fma_f32 v[78:79], v[96:97], v[78:79], v[98:99]
	s_waitcnt vmcnt(8)
	v_pk_fma_f32 v[96:97], v[154:155], v[76:77], v[104:105]
	v_pk_fma_f32 v[76:77], v[152:153], v[74:75], v[102:103]
	v_cvt_pk_bf16_f32 v74, v78, v79
	v_lshlrev_b64 v[78:79], 13, v[166:167]
	v_lshl_add_u64 v[78:79], s[10:11], 0, v[78:79]
	v_pk_fma_f32 v[80:81], v[150:151], v[80:81], v[100:101]
	v_lshl_add_u64 v[78:79], v[78:79], 0, v[130:131]
	v_cvt_pk_bf16_f32 v75, v80, v81
	v_cvt_pk_bf16_f32 v76, v76, v77
	v_cvt_pk_bf16_f32 v77, v96, v97
	global_store_dwordx4 v[78:79], v[74:77], off
	v_pk_mul_f32 v[80:81], v[140:141], v[106:107] op_sel_hi:[0,1]
	v_pk_mul_f32 v[96:97], v[140:141], v[108:109] op_sel_hi:[0,1]
	v_pk_mul_f32 v[74:75], v[140:141], v[110:111] op_sel_hi:[0,1]
	v_pk_mul_f32 v[76:77], v[140:141], v[112:113] op_sel_hi:[0,1]
	s_waitcnt vmcnt(7)
	v_pk_fma_f32 v[70:71], v[74:75], v[70:71], v[114:115]
	v_pk_fma_f32 v[74:75], v[96:97], v[68:69], v[94:95]
	v_pk_fma_f32 v[68:69], v[80:81], v[66:67], v[92:93]
	v_add_u32_e32 v92, 0x90, v146
	v_pk_fma_f32 v[72:73], v[76:77], v[72:73], v[116:117]
	v_cvt_pk_bf16_f32 v66, v70, v71
	v_ashrrev_i32_e32 v93, 31, v92
	v_cvt_pk_bf16_f32 v67, v72, v73
	v_cvt_pk_bf16_f32 v68, v68, v69
	v_cvt_pk_bf16_f32 v69, v74, v75
	global_store_dwordx4 v[78:79], v[66:69], off offset:256
	v_pk_mul_f32 v[94:95], v[138:139], v[126:127] op_sel_hi:[0,1]
	v_pk_mul_f32 v[98:99], v[138:139], v[122:123] op_sel_hi:[0,1]
	v_lshlrev_b64 v[66:67], 14, v[92:93]
	v_lshl_add_u64 v[66:67], s[0:1], 0, v[66:67]
	v_lshl_add_u64 v[78:79], v[66:67], 0, v[148:149]
	global_load_dwordx4 v[66:69], v[78:79], off nt
	global_load_dwordx4 v[70:73], v[78:79], off offset:16 nt
	global_load_dwordx4 v[74:77], v[78:79], off offset:528 nt
	s_nop 0
	global_load_dwordx4 v[78:81], v[78:79], off offset:512 nt
	v_pk_mul_f32 v[100:101], v[138:139], v[124:125] op_sel_hi:[0,1]
	v_pk_mul_f32 v[96:97], v[138:139], v[128:129] op_sel_hi:[0,1]
	v_cvt_f32_i32_e32 v29, v29
	v_cvt_f32_i32_e32 v28, v28
	v_cvt_f32_i32_e32 v26, v26
	v_cvt_f32_i32_e32 v33, v33
	v_cvt_f32_i32_e32 v32, v32
	v_cvt_f32_i32_e32 v23, v23
	v_cvt_f32_i32_e32 v22, v22
	v_cvt_f32_i32_e32 v25, v25
	v_cvt_f32_i32_e32 v24, v24
	v_cvt_f32_i32_e32 v19, v19
	v_cvt_f32_i32_e32 v21, v21
	v_cvt_f32_i32_e32 v20, v20
	v_cvt_f32_i32_e32 v18, v18
	v_cvt_f32_i32_e32 v15, v15
	v_cvt_f32_i32_e32 v14, v14
	v_cvt_f32_i32_e32 v11, v11
	v_cvt_f32_i32_e32 v13, v13
	v_cvt_f32_i32_e32 v12, v12
	v_cvt_f32_i32_e32 v10, v10
	v_cvt_f32_i32_e32 v17, v17
	v_cvt_f32_i32_e32 v16, v16
	v_cvt_f32_i32_e32 v7, v7
	v_cvt_f32_i32_e32 v6, v6
	v_cvt_f32_i32_e32 v3, v3
	v_cvt_f32_i32_e32 v5, v5
	v_cvt_f32_i32_e32 v4, v4
	v_cvt_f32_i32_e32 v2, v2
	v_cvt_f32_i32_e32 v9, v9
	v_cvt_f32_i32_e32 v8, v8
	s_andn2_b64 vcc, exec, s[6:7]
	s_mov_b64 s[6:7], -1
	s_waitcnt vmcnt(9)
	v_pk_fma_f32 v[62:63], v[94:95], v[62:63], v[82:83]
	s_waitcnt vmcnt(8)
	v_pk_fma_f32 v[82:83], v[100:101], v[60:61], v[88:89]
	v_pk_fma_f32 v[60:61], v[98:99], v[58:59], v[86:87]
	v_cvt_pk_bf16_f32 v58, v62, v63
	v_lshlrev_b64 v[62:63], 13, v[90:91]
	v_lshl_add_u64 v[62:63], s[10:11], 0, v[62:63]
	v_pk_fma_f32 v[64:65], v[96:97], v[64:65], v[84:85]
	v_lshl_add_u64 v[62:63], v[62:63], 0, v[130:131]
	v_cvt_pk_bf16_f32 v59, v64, v65
	v_cvt_pk_bf16_f32 v60, v60, v61
	v_cvt_pk_bf16_f32 v61, v82, v83
	global_store_dwordx4 v[62:63], v[58:61], off
	v_pk_mul_f32 v[82:83], v[138:139], v[108:109] op_sel_hi:[0,1]
	v_pk_mul_f32 v[64:65], v[138:139], v[106:107] op_sel_hi:[0,1]
	v_pk_mul_f32 v[58:59], v[138:139], v[110:111] op_sel_hi:[0,1]
	v_pk_mul_f32 v[60:61], v[138:139], v[112:113] op_sel_hi:[0,1]
	s_waitcnt vmcnt(7)
	v_pk_fma_f32 v[54:55], v[58:59], v[54:55], v[142:143]
	v_pk_fma_f32 v[58:59], v[82:83], v[52:53], v[120:121]
	v_add_u32_e32 v82, 0xa0, v146
	v_pk_fma_f32 v[56:57], v[60:61], v[56:57], v[144:145]
	v_pk_fma_f32 v[52:53], v[64:65], v[50:51], v[118:119]
	v_cvt_pk_bf16_f32 v50, v54, v55
	v_cvt_pk_bf16_f32 v51, v56, v57
	v_ashrrev_i32_e32 v83, 31, v82
	v_cvt_pk_bf16_f32 v52, v52, v53
	v_cvt_pk_bf16_f32 v53, v58, v59
	global_store_dwordx4 v[62:63], v[50:53], off offset:256
	v_pk_mul_f32 v[84:85], v[136:137], v[126:127] op_sel_hi:[0,1]
	v_pk_mul_f32 v[88:89], v[136:137], v[122:123] op_sel_hi:[0,1]
	v_lshlrev_b64 v[50:51], 14, v[82:83]
	v_lshl_add_u64 v[50:51], s[0:1], 0, v[50:51]
	v_lshl_add_u64 v[62:63], v[50:51], 0, v[148:149]
	v_pk_mul_f32 v[90:91], v[136:137], v[124:125] op_sel_hi:[0,1]
	global_load_dwordx4 v[50:53], v[62:63], off offset:16 nt
	global_load_dwordx4 v[54:57], v[62:63], off nt
	global_load_dwordx4 v[58:61], v[62:63], off offset:528 nt
	s_nop 0
	global_load_dwordx4 v[62:65], v[62:63], off offset:512 nt
	v_pk_mul_f32 v[86:87], v[136:137], v[128:129] op_sel_hi:[0,1]
	s_waitcnt vmcnt(9)
	v_pk_fma_f32 v[46:47], v[84:85], v[46:47], v[66:67]
	s_waitcnt vmcnt(8)
	v_pk_fma_f32 v[66:67], v[90:91], v[44:45], v[72:73]
	v_pk_fma_f32 v[44:45], v[88:89], v[42:43], v[70:71]
	v_cvt_pk_bf16_f32 v42, v46, v47
	v_lshlrev_b64 v[46:47], 13, v[92:93]
	v_lshl_add_u64 v[46:47], s[10:11], 0, v[46:47]
	v_pk_fma_f32 v[48:49], v[86:87], v[48:49], v[68:69]
	v_lshl_add_u64 v[46:47], v[46:47], 0, v[130:131]
	v_cvt_pk_bf16_f32 v43, v48, v49
	v_cvt_pk_bf16_f32 v44, v44, v45
	v_cvt_pk_bf16_f32 v45, v66, v67
	global_store_dwordx4 v[46:47], v[42:45], off
	v_pk_mul_f32 v[66:67], v[136:137], v[108:109] op_sel_hi:[0,1]
	v_pk_mul_f32 v[48:49], v[136:137], v[106:107] op_sel_hi:[0,1]
	v_pk_mul_f32 v[42:43], v[136:137], v[110:111] op_sel_hi:[0,1]
	v_pk_mul_f32 v[44:45], v[136:137], v[112:113] op_sel_hi:[0,1]
	s_waitcnt vmcnt(7)
	v_pk_fma_f32 v[38:39], v[42:43], v[38:39], v[78:79]
	v_pk_fma_f32 v[42:43], v[66:67], v[36:37], v[76:77]
	v_add_u32_e32 v66, 0xb0, v146
	v_pk_fma_f32 v[40:41], v[44:45], v[40:41], v[80:81]
	v_pk_fma_f32 v[36:37], v[48:49], v[34:35], v[74:75]
	v_cvt_pk_bf16_f32 v34, v38, v39
	v_cvt_pk_bf16_f32 v35, v40, v41
	v_ashrrev_i32_e32 v67, 31, v66
	v_cvt_pk_bf16_f32 v36, v36, v37
	v_cvt_pk_bf16_f32 v37, v42, v43
	global_store_dwordx4 v[46:47], v[34:37], off offset:256
	v_pk_mul_f32 v[68:69], v[134:135], v[126:127] op_sel_hi:[0,1]
	v_pk_mul_f32 v[72:73], v[134:135], v[122:123] op_sel_hi:[0,1]
	v_lshlrev_b64 v[34:35], 14, v[66:67]
	v_lshl_add_u64 v[34:35], s[0:1], 0, v[34:35]
	v_lshl_add_u64 v[46:47], v[34:35], 0, v[148:149]
	global_load_dwordx4 v[34:37], v[46:47], off nt
	global_load_dwordx4 v[38:41], v[46:47], off offset:16 nt
	global_load_dwordx4 v[42:45], v[46:47], off offset:528 nt
	s_nop 0
	global_load_dwordx4 v[46:49], v[46:47], off offset:512 nt
	v_pk_mul_f32 v[74:75], v[134:135], v[124:125] op_sel_hi:[0,1]
	v_pk_mul_f32 v[70:71], v[134:135], v[128:129] op_sel_hi:[0,1]
	s_waitcnt vmcnt(9)
	v_pk_fma_f32 v[52:53], v[74:75], v[28:29], v[52:53]
	s_waitcnt vmcnt(8)
	v_pk_fma_f32 v[30:31], v[68:69], v[30:31], v[54:55]
	v_pk_fma_f32 v[28:29], v[72:73], v[26:27], v[50:51]
	v_cvt_pk_bf16_f32 v26, v30, v31
	v_lshlrev_b64 v[30:31], 13, v[82:83]
	v_lshl_add_u64 v[30:31], s[10:11], 0, v[30:31]
	v_pk_fma_f32 v[32:33], v[70:71], v[32:33], v[56:57]
	v_lshl_add_u64 v[30:31], v[30:31], 0, v[130:131]
	v_cvt_pk_bf16_f32 v27, v32, v33
	v_cvt_pk_bf16_f32 v28, v28, v29
	v_cvt_pk_bf16_f32 v29, v52, v53
	global_store_dwordx4 v[30:31], v[26:29], off
	v_pk_mul_f32 v[32:33], v[134:135], v[106:107] op_sel_hi:[0,1]
	v_pk_mul_f32 v[50:51], v[134:135], v[108:109] op_sel_hi:[0,1]
	v_pk_mul_f32 v[26:27], v[134:135], v[110:111] op_sel_hi:[0,1]
	v_pk_mul_f32 v[28:29], v[134:135], v[112:113] op_sel_hi:[0,1]
	s_waitcnt vmcnt(7)
	v_pk_fma_f32 v[24:25], v[28:29], v[24:25], v[64:65]
	v_pk_fma_f32 v[22:23], v[26:27], v[22:23], v[62:63]
	v_pk_fma_f32 v[26:27], v[50:51], v[20:21], v[60:61]
	v_pk_fma_f32 v[20:21], v[32:33], v[18:19], v[58:59]
	v_cvt_pk_bf16_f32 v18, v22, v23
	v_cvt_pk_bf16_f32 v19, v24, v25
	v_pk_mul_f32 v[22:23], v[132:133], v[122:123] op_sel_hi:[0,1]
	v_cvt_pk_bf16_f32 v20, v20, v21
	v_cvt_pk_bf16_f32 v21, v26, v27
	global_store_dwordx4 v[30:31], v[18:21], off offset:256
	v_pk_mul_f32 v[24:25], v[132:133], v[124:125] op_sel_hi:[0,1]
	s_nop 0
	v_pk_mul_f32 v[18:19], v[126:127], v[132:133] op_sel_hi:[1,0]
	v_pk_mul_f32 v[20:21], v[128:129], v[132:133] op_sel_hi:[1,0]
	s_waitcnt vmcnt(5)
	v_pk_fma_f32 v[14:15], v[18:19], v[14:15], v[34:35]
	s_waitcnt vmcnt(4)
	v_pk_fma_f32 v[18:19], v[24:25], v[12:13], v[40:41]
	v_pk_fma_f32 v[12:13], v[22:23], v[10:11], v[38:39]
	v_cvt_pk_bf16_f32 v10, v14, v15
	v_lshlrev_b64 v[14:15], 13, v[66:67]
	v_lshl_add_u64 v[14:15], s[10:11], 0, v[14:15]
	v_pk_fma_f32 v[16:17], v[20:21], v[16:17], v[36:37]
	v_lshl_add_u64 v[14:15], v[14:15], 0, v[130:131]
	v_cvt_pk_bf16_f32 v11, v16, v17
	v_cvt_pk_bf16_f32 v12, v12, v13
	v_cvt_pk_bf16_f32 v13, v18, v19
	global_store_dwordx4 v[14:15], v[10:13], off
	v_pk_mul_f32 v[16:17], v[132:133], v[106:107] op_sel_hi:[0,1]
	v_pk_mul_f32 v[18:19], v[132:133], v[108:109] op_sel_hi:[0,1]
	v_pk_mul_f32 v[10:11], v[132:133], v[110:111] op_sel_hi:[0,1]
	v_pk_mul_f32 v[12:13], v[132:133], v[112:113] op_sel_hi:[0,1]
	s_waitcnt vmcnt(3)
	v_pk_fma_f32 v[6:7], v[10:11], v[6:7], v[46:47]
	v_pk_fma_f32 v[10:11], v[18:19], v[4:5], v[44:45]
	v_pk_fma_f32 v[4:5], v[16:17], v[2:3], v[42:43]
	v_pk_fma_f32 v[8:9], v[12:13], v[8:9], v[48:49]
	v_cvt_pk_bf16_f32 v2, v6, v7
	s_nop 0
	v_cvt_pk_bf16_f32 v3, v8, v9
	v_cvt_pk_bf16_f32 v4, v4, v5
	v_cvt_pk_bf16_f32 v5, v10, v11
	global_store_dwordx4 v[14:15], v[2:5], off offset:256
	s_cbranch_vccnz .LBB0_1173
	s_andn2_b64 vcc, exec, s[2:3]
	s_cbranch_vccnz .LBB0_1172
	s_barrier
	s_branch .LBB0_1172

	.amdhsa_kernel _Z3fwd4Args
		.amdhsa_group_segment_fixed_size 0
		.amdhsa_private_segment_fixed_size 0
		.amdhsa_kernarg_size 464
		.amdhsa_user_sgpr_count 2
		.amdhsa_user_sgpr_dispatch_ptr 0
		.amdhsa_user_sgpr_queue_ptr 0
		.amdhsa_user_sgpr_kernarg_segment_ptr 1
		.amdhsa_user_sgpr_dispatch_id 0
		.amdhsa_user_sgpr_kernarg_preload_length 0
		.amdhsa_user_sgpr_kernarg_preload_offset 0
		.amdhsa_user_sgpr_private_segment_size 0
		.amdhsa_uses_dynamic_stack 0
		.amdhsa_enable_private_segment 0
		.amdhsa_system_sgpr_workgroup_id_x 1
		.amdhsa_system_sgpr_workgroup_id_y 0
		.amdhsa_system_sgpr_workgroup_id_z 0
		.amdhsa_system_sgpr_workgroup_info 0
		.amdhsa_system_vgpr_workitem_id 0
		.amdhsa_next_free_vgpr 256
		.amdhsa_next_free_sgpr 100
		.amdhsa_accum_offset 256
		.amdhsa_reserve_vcc 1
		.amdhsa_float_round_mode_32 0
		.amdhsa_float_round_mode_16_64 0
		.amdhsa_float_denorm_mode_32 3
		.amdhsa_float_denorm_mode_16_64 3
		.amdhsa_dx10_clamp 1
		.amdhsa_ieee_mode 1
		.amdhsa_fp16_overflow 0
		.amdhsa_tg_split 0
		.amdhsa_exception_fp_ieee_invalid_op 0
		.amdhsa_exception_fp_denorm_src 0
		.amdhsa_exception_fp_ieee_div_zero 0
		.amdhsa_exception_fp_ieee_overflow 0
		.amdhsa_exception_fp_ieee_underflow 0
		.amdhsa_exception_fp_ieee_inexact 0
		.amdhsa_exception_int_div_zero 0
	.end_amdhsa_kernel

amdhsa.kernels:
  - .agpr_count:     0
    .args:
      - .offset:         0
        .size:           208
        .value_kind:     by_value
      - .offset:         208
        .size:           4
        .value_kind:     hidden_block_count_x
      - .offset:         212
        .size:           4
        .value_kind:     hidden_block_count_y
      - .offset:         216
        .size:           4
        .value_kind:     hidden_block_count_z
      - .offset:         220
        .size:           2
        .value_kind:     hidden_group_size_x
      - .offset:         222
        .size:           2
        .value_kind:     hidden_group_size_y
      - .offset:         224
        .size:           2
        .value_kind:     hidden_group_size_z
      - .offset:         226
        .size:           2
        .value_kind:     hidden_remainder_x
      - .offset:         228
        .size:           2
        .value_kind:     hidden_remainder_y
      - .offset:         230
        .size:           2
        .value_kind:     hidden_remainder_z
      - .offset:         248
        .size:           8
        .value_kind:     hidden_global_offset_x
      - .offset:         256
        .size:           8
        .value_kind:     hidden_global_offset_y
      - .offset:         264
        .size:           8
        .value_kind:     hidden_global_offset_z
      - .offset:         272
        .size:           2
        .value_kind:     hidden_grid_dims
      - .offset:         328
        .size:           4
        .value_kind:     hidden_dynamic_lds_size
    .group_segment_fixed_size: 0
    .kernarg_segment_align: 8
    .kernarg_segment_size: 464
    .language:       OpenCL C
    .language_version:
      - 2
      - 0
    .max_flat_workgroup_size: 512
    .name:           _Z3fwd4Args
    .private_segment_fixed_size: 0
    .sgpr_count:     106
    .sgpr_spill_count: 70
    .symbol:         _Z3fwd4Args.kd
    .uniform_work_group_size: 1
    .uses_dynamic_stack: false
    .vgpr_count:     256
    .vgpr_spill_count: 0
    .wavefront_size: 64
